# router tails: workgroup barrier between the ticket computation and the base publish removed (the publish block no longer reads LDS written by other threads); on top of v62
# baseline (speedup 1.0000x reference)
.LBB0_936:
	s_or_b64 exec, exec, s[10:11]
	s_waitcnt lgkmcnt(0)
	s_and_saveexec_b64 s[8:9], s[6:7]
	s_cbranch_execz .LBB0_940
	v_lshl_add_u32 v1, v0, 2, 0
	v_add_u32_e32 v1, 0x1ee00, v1
	s_waitcnt vmcnt(0)
	ds_write_b32 v1, v72

.LBB0_1983:
	s_or_b64 exec, exec, s[10:11]
	s_waitcnt lgkmcnt(0)
	s_and_saveexec_b64 s[2:3], s[6:7]
	s_cbranch_execz .LBB0_1987
	v_lshl_add_u32 v1, v0, 2, 0
	v_add_u32_e32 v1, 0x1ee00, v1
	s_waitcnt vmcnt(0)
	ds_write_b32 v1, v72
